# weight-conversion runs keep two tiles in flight (loads of the tile after next issued into the register set just drained, before convert/store); rest as previous version
# speedup vs baseline: 1.0134x; 1.0020x over previous
; #define LAS __attribute__((address_space(3)))
; __device__ __forceinline__ void tr_tile8(const float* __restrict__ src, int N, const float* __restrict__ ksc, float wscale, unsigned char* __restrict__ dst, int ldd, int k0, int n0, int drow0, LAS unsigned* tl, int tid) {
;     const int c4 = (tid & 15) * 4, kq = tid >> 4;
;     const float* s0 = src + (size_t)(k0 + 4 * kq) * N + n0 + c4;
;     f32x4 a = *(const f32x4*)s0, b = *(const f32x4*)(s0 + N), c = *(const f32x4*)(s0 + 2 * (size_t)N), d = *(const f32x4*)(s0 + 3 * (size_t)N);
;     float sa = wscale, sb = wscale, sc = wscale, sd = wscale;
;     if (ksc) { sa *= ksc[k0 + 4 * kq]; sb *= ksc[k0 + 4 * kq + 1]; sc *= ksc[k0 + 4 * kq + 2]; sd *= ksc[k0 + 4 * kq + 3]; }
; #pragma unroll
;     for (int j = 0; j < 4; ++j) tl[(c4 + j) * 33 + kq] = pk4_fp8(a[j] * sa, b[j] * sb, c[j] * sc, d[j] * sd);
;     __syncthreads();
;     const int n = tid >> 3, seg = tid & 7;
;     unsigned w[4];
; #pragma unroll
;     for (int q = 0; q < 4; ++q) w[q] = tl[n * 33 + seg * 4 + q];
;     *(u32x4*)(dst + (size_t)(drow0 + n) * ldd + k0 + seg * 16) = (u32x4){w[0], w[1], w[2], w[3]};
;     __syncthreads();
; __device__ __forceinline__ void phase_prologue(kcu64_t* ka, unsigned char* ws, LAS unsigned char* lds, int G, int bid, int tid, int jlo, int jhi, bool do_x) {
;     ...
;     for (int t = t_lo + bid; t < t_hi; t += G) {
.LBB0_406:
	s_waitcnt vmcnt(0)
	s_mov_b32 s101, 0
	s_cmp_lt_i32 s100, 0
	s_cbranch_scc1 .Lcv1_nx
	s_cmp_lt_i32 s23, 30
	s_cbranch_scc0 .Lcv1_nx
	s_cmp_eq_u32 s50, 0x100
	s_cbranch_scc0 .Lcv1_nx
	s_mov_b64 vcc, 0x800000
	v_lshl_add_u64 v[64:65], v[64:65], 0, vcc
	s_lshl_b64 s[48:49], s[36:37], 2
	v_lshl_add_u64 v[72:73], v[64:65], 0, s[48:49]
	global_load_dwordx4 v[80:83], v[64:65], off
	global_load_dwordx4 v[84:87], v[72:73], off
	v_lshl_add_u64 v[72:73], v[72:73], 0, s[48:49]
	v_lshl_add_u64 v[74:75], v[72:73], 0, s[48:49]
	global_load_dwordx4 v[88:91], v[72:73], off
	global_load_dwordx4 v[92:95], v[74:75], off
	s_mov_b32 s101, 1
	s_cmp_lt_i32 s23, 28
	s_cbranch_scc0 .Lcv1_nx
	s_mov_b64 vcc, 0x800000
	v_lshl_add_u64 v[64:65], v[64:65], 0, vcc
	s_lshl_b64 s[48:49], s[36:37], 2
	v_lshl_add_u64 v[72:73], v[64:65], 0, s[48:49]
	global_load_dwordx4 v[96:99], v[64:65], off
	global_load_dwordx4 v[100:103], v[72:73], off
	v_lshl_add_u64 v[72:73], v[72:73], 0, s[48:49]
	v_lshl_add_u64 v[74:75], v[72:73], 0, s[48:49]
	global_load_dwordx4 v[104:107], v[72:73], off
	global_load_dwordx4 v[108:111], v[74:75], off
	s_mov_b32 s101, 2
.Lcv1_nx:
	v_mul_f32_e32 v8, v8, v22
	v_mul_f32_e32 v12, v12, v23
	v_cvt_pk_fp8_f32 v8, v8, v12
	v_mul_f32_e32 v9, v9, v22
	v_mul_f32_e32 v12, v13, v23
	v_cvt_pk_fp8_f32 v9, v9, v12
	s_lshl_b32 s8, s25, 7
	s_and_b32 s8, s8, 0xffffff00
	v_mul_f32_e32 v0, v0, v20
	v_mul_f32_e32 v4, v4, v21
	s_and_b32 s9, s58, 64
	s_or_b32 s8, s8, s29
	v_cvt_pk_fp8_f32 v8, v0, v4 op_sel:[0,0,1]
	v_mul_f32_e32 v0, v1, v20
	v_mul_f32_e32 v1, v5, v21
	s_or_b32 s25, s8, s9
	v_cvt_pk_fp8_f32 v9, v0, v1 op_sel:[0,0,1]
	v_mul_f32_e32 v0, v10, v22
	v_mul_f32_e32 v1, v14, v23
	s_and_b64 s[8:9], s[56:57], exec
	v_cvt_pk_fp8_f32 v0, v0, v1
	v_mul_f32_e32 v1, v11, v22
	v_mul_f32_e32 v5, v15, v23
	s_mul_i32 s8, s62, s24
	s_mul_hi_u32 s9, s62, s23
	v_cvt_pk_fp8_f32 v1, v1, v5
	s_cselect_b32 s25, s58, s25
	s_add_i32 s8, s9, s8
	s_mul_i32 s9, s63, s23
	s_add_i32 s9, s8, s9
	s_mul_i32 s8, s62, s23
	v_mul_f32_e32 v2, v2, v20
	v_mul_f32_e32 v4, v6, v21
	v_cvt_pk_fp8_f32 v0, v2, v4 op_sel:[0,0,1]
	v_mul_f32_e32 v2, v3, v20
	v_mul_f32_e32 v3, v7, v21
	s_add_u32 s8, s42, s8
	v_cvt_pk_fp8_f32 v1, v2, v3 op_sel:[0,0,1]
	s_addc_u32 s9, s43, s9
	v_add_u32_e32 v6, s25, v24
	v_mov_b64_e32 v[4:5], s[8:9]
	v_mad_u64_u32 v[4:5], s[8:9], v6, s28, v[4:5]
	ds_write2_b32 v25, v8, v9 offset1:33
	ds_write2_b32 v25, v0, v1 offset0:66 offset1:99
	s_waitcnt lgkmcnt(0)
	s_barrier
	ds_read2_b32 v[0:1], v26 offset1:1
	ds_read2_b32 v[2:3], v26 offset0:2 offset1:3
	v_ashrrev_i32_e32 v7, 31, v6
	v_mov_b32_e32 v6, v5
	v_mad_u64_u32 v[6:7], s[8:9], v7, s28, v[6:7]
	v_mov_b32_e32 v5, v6
	s_ashr_i32 s41, s40, 31
	v_lshl_add_u64 v[4:5], v[4:5], 0, s[40:41]
	s_add_i32 s15, s15, s50
	v_readlane_b32 s49, v255, 49
	s_mov_b64 s[86:87], 0x5000
	v_lshl_add_u64 v[4:5], v[4:5], 0, v[18:19]
	s_cmpk_gt_i32 s15, 0x6cef
	s_waitcnt lgkmcnt(0)
	global_store_dwordx4 v[4:5], v[0:3], off
	s_barrier
	s_cbranch_scc1 .LBB0_447
	s_cmp_eq_u32 s101, 0
	s_cbranch_scc1 .LBB0_407
	s_add_i32 s23, s23, 2
	s_mov_b32 s25, s100
	s_sub_u32 s101, s101, 1
	s_branch .Lcv1_f0
.Lcv1_f0:
	s_cmp_eq_u32 s101, 1
	s_cbranch_scc1 .Lcv1_f0w5
	s_waitcnt vmcnt(1)
	s_branch .Lcv1_f0m
.Lcv1_f0w5:
	s_waitcnt vmcnt(5)
.Lcv1_f0m:
	v_mov_b64_e32 v[8:9], v[80:81]
	v_mov_b64_e32 v[10:11], v[82:83]
	v_mov_b64_e32 v[12:13], v[84:85]
	v_mov_b64_e32 v[14:15], v[86:87]
	v_mov_b64_e32 v[0:1], v[88:89]
	v_mov_b64_e32 v[2:3], v[90:91]
	v_mov_b64_e32 v[4:5], v[92:93]
	v_mov_b64_e32 v[6:7], v[94:95]
	s_cmp_eq_u32 s101, 1
	s_cbranch_scc0 .Lcv1_f0p
	s_cmp_lt_i32 s23, 28
	s_cbranch_scc0 .Lcv1_f0p
	s_mov_b64 vcc, 0x800000
	v_lshl_add_u64 v[64:65], v[64:65], 0, vcc
	s_lshl_b64 s[48:49], s[36:37], 2
	v_lshl_add_u64 v[72:73], v[64:65], 0, s[48:49]
	global_load_dwordx4 v[80:83], v[64:65], off
	global_load_dwordx4 v[84:87], v[72:73], off
	v_lshl_add_u64 v[72:73], v[72:73], 0, s[48:49]
	v_lshl_add_u64 v[74:75], v[72:73], 0, s[48:49]
	global_load_dwordx4 v[88:91], v[72:73], off
	global_load_dwordx4 v[92:95], v[74:75], off
	s_mov_b32 s101, 2

; #define LAS __attribute__((address_space(3)))
; __device__ __forceinline__ void tr_tile8(const float* __restrict__ src, int N, const float* __restrict__ ksc, float wscale, unsigned char* __restrict__ dst, int ldd, int k0, int n0, int drow0, LAS unsigned* tl, int tid) {
;     const int c4 = (tid & 15) * 4, kq = tid >> 4;
;     const float* s0 = src + (size_t)(k0 + 4 * kq) * N + n0 + c4;
;     f32x4 a = *(const f32x4*)s0, b = *(const f32x4*)(s0 + N), c = *(const f32x4*)(s0 + 2 * (size_t)N), d = *(const f32x4*)(s0 + 3 * (size_t)N);
; __device__ __forceinline__ void phase_prologue(kcu64_t* ka, unsigned char* ws, LAS unsigned char* lds, int G, int bid, int tid, int jlo, int jhi, bool do_x) {
;     ...
;     for (int t = t_lo + bid; t < t_hi; t += G) {
.Lcv1_f1m:
	v_mov_b64_e32 v[8:9], v[96:97]
	v_mov_b64_e32 v[10:11], v[98:99]
	v_mov_b64_e32 v[12:13], v[100:101]
	v_mov_b64_e32 v[14:15], v[102:103]
	v_mov_b64_e32 v[0:1], v[104:105]
	v_mov_b64_e32 v[2:3], v[106:107]
	v_mov_b64_e32 v[4:5], v[108:109]
	v_mov_b64_e32 v[6:7], v[110:111]
	s_cmp_eq_u32 s101, 1
	s_cbranch_scc0 .Lcv1_f1p
	s_cmp_lt_i32 s23, 28
	s_cbranch_scc0 .Lcv1_f1p
	s_mov_b64 vcc, 0x800000
	v_lshl_add_u64 v[64:65], v[64:65], 0, vcc
	s_lshl_b64 s[48:49], s[36:37], 2
	v_lshl_add_u64 v[72:73], v[64:65], 0, s[48:49]
	global_load_dwordx4 v[96:99], v[64:65], off
	global_load_dwordx4 v[100:103], v[72:73], off
	v_lshl_add_u64 v[72:73], v[72:73], 0, s[48:49]
	v_lshl_add_u64 v[74:75], v[72:73], 0, s[48:49]
	global_load_dwordx4 v[104:107], v[72:73], off
	global_load_dwordx4 v[108:111], v[74:75], off
	s_mov_b32 s101, 2

; #define LAS __attribute__((address_space(3)))
; __device__ __forceinline__ void tr_tile8(const float* __restrict__ src, int N, const float* __restrict__ ksc, float wscale, unsigned char* __restrict__ dst, int ldd, int k0, int n0, int drow0, LAS unsigned* tl, int tid) {
;     const int c4 = (tid & 15) * 4, kq = tid >> 4;
;     const float* s0 = src + (size_t)(k0 + 4 * kq) * N + n0 + c4;
;     f32x4 a = *(const f32x4*)s0, b = *(const f32x4*)(s0 + N), c = *(const f32x4*)(s0 + 2 * (size_t)N), d = *(const f32x4*)(s0 + 3 * (size_t)N);
;     float sa = wscale, sb = wscale, sc = wscale, sd = wscale;
;     if (ksc) { sa *= ksc[k0 + 4 * kq]; sb *= ksc[k0 + 4 * kq + 1]; sc *= ksc[k0 + 4 * kq + 2]; sd *= ksc[k0 + 4 * kq + 3]; }
; #pragma unroll
;     for (int j = 0; j < 4; ++j) tl[(c4 + j) * 33 + kq] = pk4_fp8(a[j] * sa, b[j] * sb, c[j] * sc, d[j] * sd);
;     __syncthreads();
;     const int n = tid >> 3, seg = tid & 7;
;     unsigned w[4];
; #pragma unroll
;     for (int q = 0; q < 4; ++q) w[q] = tl[n * 33 + seg * 4 + q];
;     *(u32x4*)(dst + (size_t)(drow0 + n) * ldd + k0 + seg * 16) = (u32x4){w[0], w[1], w[2], w[3]};
;     __syncthreads();
.Lcv2_nx:
	v_mul_f32_e32 v8, v8, v22
	v_mul_f32_e32 v12, v12, v23
	v_cvt_pk_fp8_f32 v8, v8, v12
	v_mul_f32_e32 v9, v9, v22
	v_mul_f32_e32 v12, v13, v23
	v_cvt_pk_fp8_f32 v9, v9, v12
	s_lshl_b32 s8, s25, 7
	s_and_b32 s8, s8, 0xffffff00
	v_mul_f32_e32 v0, v0, v20
	v_mul_f32_e32 v4, v4, v21
	s_and_b32 s9, s60, 64
	s_or_b32 s8, s8, s29
	v_cvt_pk_fp8_f32 v8, v0, v4 op_sel:[0,0,1]
	v_mul_f32_e32 v0, v1, v20
	v_mul_f32_e32 v1, v5, v21
	s_or_b32 s25, s8, s9
	v_cvt_pk_fp8_f32 v9, v0, v1 op_sel:[0,0,1]
	v_mul_f32_e32 v0, v10, v22
	v_mul_f32_e32 v1, v14, v23
	s_and_b64 s[8:9], s[56:57], exec
	v_cvt_pk_fp8_f32 v0, v0, v1
	v_mul_f32_e32 v1, v11, v22
	v_mul_f32_e32 v5, v15, v23
	s_mul_i32 s8, s62, s24
	s_mul_hi_u32 s9, s62, s23
	v_cvt_pk_fp8_f32 v1, v1, v5
	s_cselect_b32 s25, s60, s25
	s_add_i32 s8, s9, s8
	s_mul_i32 s9, s63, s23
	s_add_i32 s9, s8, s9
	s_mul_i32 s8, s62, s23
	v_mul_f32_e32 v2, v2, v20
	v_mul_f32_e32 v4, v6, v21
	v_cvt_pk_fp8_f32 v0, v2, v4 op_sel:[0,0,1]
	v_mul_f32_e32 v2, v3, v20
	v_mul_f32_e32 v3, v7, v21
	s_add_u32 s8, s54, s8
	v_cvt_pk_fp8_f32 v1, v2, v3 op_sel:[0,0,1]
	s_addc_u32 s9, s55, s9
	v_add_u32_e32 v6, s25, v24
	v_mov_b64_e32 v[4:5], s[8:9]
	v_mad_u64_u32 v[4:5], s[8:9], v6, s28, v[4:5]
	ds_write2_b32 v25, v8, v9 offset1:33
	ds_write2_b32 v25, v0, v1 offset0:66 offset1:99
	s_waitcnt lgkmcnt(0)
	s_barrier
	ds_read2_b32 v[0:1], v26 offset1:1
	ds_read2_b32 v[2:3], v26 offset0:2 offset1:3
	v_ashrrev_i32_e32 v7, 31, v6
	v_mov_b32_e32 v6, v5
	v_mad_u64_u32 v[6:7], s[8:9], v7, s28, v[6:7]
	v_mov_b32_e32 v5, v6
	s_ashr_i32 s59, s58, 31
	v_lshl_add_u64 v[4:5], v[4:5], 0, s[58:59]
	s_add_i32 s15, s15, s50
	v_readlane_b32 s49, v255, 49
	s_mov_b64 s[86:87], 0x5000
	v_lshl_add_u64 v[4:5], v[4:5], 0, v[18:19]
	s_cmpk_gt_i32 s15, 0x6cef
	s_waitcnt lgkmcnt(0)
	global_store_dwordx4 v[4:5], v[0:3], off
	s_barrier
	s_cbranch_scc1 .LBB0_629
	s_cmp_eq_u32 s101, 0
	s_cbranch_scc1 .LBB0_589
	s_add_i32 s23, s23, 2
	s_mov_b32 s25, s100
	s_sub_u32 s101, s101, 1
	s_branch .Lcv2_f0
